# speedup vs baseline: 1.0049x; 1.0049x over previous
_Z13gather_kernelPK15HIP_vector_typeIjLj2EEPKiPK6OvfRecPKDF16_PKfPDF16_:
	s_lshr_b32 s3, s2, 2
	s_and_b32 s3, s3, 0x3ffffffe
	s_and_b32 s4, s2, 1
	s_or_b32 s3, s3, s4
	s_cmpk_gt_u32 s3, 0x186
	s_cbranch_scc1 .LBB1_156
	s_load_dwordx4 s[8:11], s[0:1], 0x0
	s_movk_i32 s4, 0x80
	s_lshl_b32 s12, s3, 4
	s_addk_i32 s12, 0x800
	v_lshrrev_b32_e32 v2, 6, v0
	v_cmp_gt_u32_e64 s[4:5], s4, v0
	v_lshlrev_b32_e32 v1, 2, v0
	v_readfirstlane_b32 s62, v2
	s_and_saveexec_b64 s[6:7], s[4:5]
	v_mov_b32_e32 v2, 0
	ds_write_b32 v1, v2 offset:10832
	s_or_b64 exec, exec, s[6:7]
	s_waitcnt lgkmcnt(0)
	v_cmp_gt_u32_e64 s[6:7], 64, v0
	s_and_saveexec_b64 s[12:13], s[6:7]
	v_mov_b32_e32 v2, 0
	ds_write_b32 v1, v2 offset:11856
	s_or_b64 exec, exec, s[12:13]
	s_waitcnt lgkmcnt(0)
	s_mul_i32 s15, s3, 0x5000
	s_mul_hi_u32 s13, s3, 0x5000
	s_add_u32 s8, s8, s15
	s_addc_u32 s9, s9, s13
	v_lshlrev_b32_e32 v2, 3, v0
	v_mov_b32_e32 v3, 0
	v_lshl_add_u64 v[4:5], s[8:9], 0, v[2:3]
	s_movk_i32 s13, 0x1000
	s_barrier
	global_load_dwordx2 v[20:21], v2, s[8:9]
	global_load_dwordx2 v[18:19], v2, s[8:9] offset:2048
	v_add_co_u32_e32 v2, vcc, s13, v4
	s_movk_i32 s13, 0x2000
	s_nop 0
	v_addc_co_u32_e32 v3, vcc, 0, v5, vcc
	v_add_co_u32_e32 v6, vcc, s13, v4
	s_movk_i32 s13, 0x3000
	s_nop 0
	v_addc_co_u32_e32 v7, vcc, 0, v5, vcc
	v_add_co_u32_e32 v24, vcc, s13, v4
	v_or_b32_e32 v23, 0x400, v0
	s_nop 0
	v_addc_co_u32_e32 v25, vcc, 0, v5, vcc
	v_lshlrev_b32_e32 v8, 3, v23
	v_or_b32_e32 v22, 0x800, v0
	v_add_co_u32_e32 v26, vcc, 0x4000, v4
	global_load_dwordx2 v[16:17], v[2:3], off
	global_load_dwordx2 v[14:15], v[2:3], off offset:2048
	global_load_dwordx2 v[12:13], v8, s[8:9]
	global_load_dwordx2 v[10:11], v[6:7], off offset:2048
	v_lshlrev_b32_e32 v28, 3, v22
	v_addc_co_u32_e32 v27, vcc, 0, v5, vcc
	global_load_dwordx2 v[8:9], v[24:25], off
	global_load_dwordx2 v[6:7], v[24:25], off offset:2048
	global_load_dwordx2 v[4:5], v28, s[8:9]
	global_load_dwordx2 v[2:3], v[26:27], off offset:2048
	s_lshl_b32 s51, s3, 4
	s_addk_i32 s51, 0x800
	s_load_dwordx4 s[36:39], s[10:11], s51 offset:0x0
	v_mov_b32_e32 v54, 1
	s_waitcnt lgkmcnt(0)
	s_min_u32 s36, s36, 0x280
	s_min_u32 s37, s37, 0x280
	s_min_u32 s38, s38, 0x280
	s_min_u32 s39, s39, 0x280
	s_addk_i32 s37, 0x280
	s_addk_i32 s38, 0x500
	s_addk_i32 s39, 0x780
	s_cmp_ge_u32 s62, 2
	s_cselect_b32 s54, s37, s36
	s_cselect_b32 s59, s39, s38
	s_mov_b32 s52, s36
	s_mov_b32 s53, s36
	s_mov_b32 s55, s37
	s_mov_b32 s56, s37
	s_mov_b32 s57, s38
	s_mov_b32 s58, s38
	s_mov_b32 s60, s39
	s_mov_b32 s61, s39
	v_cmp_gt_i32_e32 vcc, s52, v0
	s_and_saveexec_b64 s[8:9], vcc
	s_waitcnt vmcnt(9)
	v_lshrrev_b32_e32 v33, 16, v20
	v_lshlrev_b32_e32 v53, 2, v33
	ds_add_rtn_u32 v43, v53, v54 offset:10832
	s_or_b64 exec, exec, s[8:9]
	v_or_b32_e32 v55, 0x100, v0
	v_cmp_gt_i32_e32 vcc, s53, v55
	s_and_saveexec_b64 s[8:9], vcc
	s_waitcnt vmcnt(8)
	v_lshrrev_b32_e32 v34, 16, v18
	v_lshlrev_b32_e32 v53, 2, v34
	ds_add_rtn_u32 v44, v53, v54 offset:10832
	s_or_b64 exec, exec, s[8:9]
	v_or_b32_e32 v55, 0x200, v0
	v_cmp_gt_i32_e32 vcc, s54, v55
	s_and_saveexec_b64 s[8:9], vcc
	s_waitcnt vmcnt(7)
	v_lshrrev_b32_e32 v35, 16, v16
	v_lshlrev_b32_e32 v53, 2, v35
	ds_add_rtn_u32 v45, v53, v54 offset:10832
	s_or_b64 exec, exec, s[8:9]
	v_or_b32_e32 v55, 0x300, v0
	v_cmp_gt_i32_e32 vcc, s55, v55
	s_and_saveexec_b64 s[8:9], vcc
	s_waitcnt vmcnt(6)
	v_lshrrev_b32_e32 v36, 16, v14
	v_lshlrev_b32_e32 v53, 2, v36
	ds_add_rtn_u32 v46, v53, v54 offset:10832
	s_or_b64 exec, exec, s[8:9]
	v_or_b32_e32 v55, 0x400, v0
	v_cmp_gt_i32_e32 vcc, s56, v55
	s_and_saveexec_b64 s[8:9], vcc
	s_waitcnt vmcnt(5)
	v_lshrrev_b32_e32 v37, 16, v12
	v_lshlrev_b32_e32 v53, 2, v37
	ds_add_rtn_u32 v47, v53, v54 offset:10832
	s_or_b64 exec, exec, s[8:9]
	v_or_b32_e32 v55, 0x500, v0
	v_cmp_gt_i32_e32 vcc, s57, v55
	s_and_saveexec_b64 s[8:9], vcc
	s_waitcnt vmcnt(4)
	v_lshrrev_b32_e32 v38, 16, v10
	v_lshlrev_b32_e32 v53, 2, v38
	ds_add_rtn_u32 v48, v53, v54 offset:10832
	s_or_b64 exec, exec, s[8:9]
	v_or_b32_e32 v55, 0x600, v0
	v_cmp_gt_i32_e32 vcc, s58, v55
	s_and_saveexec_b64 s[8:9], vcc
	s_waitcnt vmcnt(3)
	v_lshrrev_b32_e32 v39, 16, v8
	v_lshlrev_b32_e32 v53, 2, v39
	ds_add_rtn_u32 v49, v53, v54 offset:10832
	s_or_b64 exec, exec, s[8:9]
	v_or_b32_e32 v55, 0x700, v0
	v_cmp_gt_i32_e32 vcc, s59, v55
	s_and_saveexec_b64 s[8:9], vcc
	s_waitcnt vmcnt(2)
	v_lshrrev_b32_e32 v40, 16, v6
	v_lshlrev_b32_e32 v53, 2, v40
	ds_add_rtn_u32 v50, v53, v54 offset:10832
	s_or_b64 exec, exec, s[8:9]
	v_or_b32_e32 v55, 0x800, v0
	v_cmp_gt_i32_e32 vcc, s60, v55
	s_and_saveexec_b64 s[8:9], vcc
	s_waitcnt vmcnt(1)
	v_lshrrev_b32_e32 v41, 16, v4
	v_lshlrev_b32_e32 v53, 2, v41
	ds_add_rtn_u32 v51, v53, v54 offset:10832
	s_or_b64 exec, exec, s[8:9]
	v_or_b32_e32 v55, 0x900, v0
	v_cmp_gt_i32_e32 vcc, s61, v55
	s_and_saveexec_b64 s[8:9], vcc
	s_waitcnt vmcnt(0)
	v_lshrrev_b32_e32 v42, 16, v2
	v_lshlrev_b32_e32 v53, 2, v42
	ds_add_rtn_u32 v52, v53, v54 offset:10832
	s_or_b64 exec, exec, s[8:9]
	s_waitcnt lgkmcnt(0)
	v_cmp_gt_i32_e32 vcc, s52, v0
	v_lshl_or_b32 v56, v43, 8, v33
	s_nop 0
	v_cndmask_b32_e32 v32, -1, v56, vcc
	v_or_b32_e32 v55, 0x100, v0
	v_cmp_gt_i32_e32 vcc, s53, v55
	v_lshl_or_b32 v56, v44, 8, v34
	s_nop 0
	v_cndmask_b32_e32 v27, -1, v56, vcc
	v_or_b32_e32 v55, 0x200, v0
	v_cmp_gt_i32_e32 vcc, s54, v55
	v_lshl_or_b32 v56, v45, 8, v35
	s_nop 0
	v_cndmask_b32_e32 v31, -1, v56, vcc
	v_or_b32_e32 v55, 0x300, v0
	v_cmp_gt_i32_e32 vcc, s55, v55
	v_lshl_or_b32 v56, v46, 8, v36
	s_nop 0
	v_cndmask_b32_e32 v26, -1, v56, vcc
	v_or_b32_e32 v55, 0x400, v0
	v_cmp_gt_i32_e32 vcc, s56, v55
	v_lshl_or_b32 v56, v47, 8, v37
	s_nop 0
	v_cndmask_b32_e32 v30, -1, v56, vcc
	v_or_b32_e32 v55, 0x500, v0
	v_cmp_gt_i32_e32 vcc, s57, v55
	v_lshl_or_b32 v56, v48, 8, v38
	s_nop 0
	v_cndmask_b32_e32 v24, -1, v56, vcc
	v_or_b32_e32 v55, 0x600, v0
	v_cmp_gt_i32_e32 vcc, s58, v55
	v_lshl_or_b32 v56, v49, 8, v39
	s_nop 0
	v_cndmask_b32_e32 v29, -1, v56, vcc
	v_or_b32_e32 v55, 0x700, v0
	v_cmp_gt_i32_e32 vcc, s59, v55
	v_lshl_or_b32 v56, v50, 8, v40
	s_nop 0
	v_cndmask_b32_e32 v23, -1, v56, vcc
	v_or_b32_e32 v55, 0x800, v0
	v_cmp_gt_i32_e32 vcc, s60, v55
	v_lshl_or_b32 v56, v51, 8, v41
	s_nop 0
	v_cndmask_b32_e32 v28, -1, v56, vcc
	v_or_b32_e32 v55, 0x900, v0
	v_cmp_gt_i32_e32 vcc, s61, v55
	v_lshl_or_b32 v56, v52, 8, v42
	s_nop 0
	v_cndmask_b32_e32 v22, -1, v56, vcc
